# QKV GEMM K-loop: first iteration peeled with SrcC=0 (rotation-aware), 128 accumulator-zeroing v_mov per unit removed
# speedup vs baseline: 1.0023x; 1.0023x over previous
; #define PG8_STAGE(bufoff, gbase, voff) do { _Pragma("unroll") for (int _i = 0; _i < 2; ++_i) \
;         __builtin_amdgcn_global_load_lds((const unsigned*)((const char*)(gbase) + (voff)[_i]), (PG8_LAS unsigned*)(lds + (bufoff) + ldsw + _i * 8192), 16, 0, 0); } while (0)
; #define PG8_LDA(dst, b, h) do { _Pragma("unroll") for (int m = 0; m < 4; ++m) _Pragma("unroll") for (int k = 0; k < 2; ++k) dst[m][k] = *(const PG8_LAS bf16x8*)(lds + PG8_SA(b, h) + aoff + m * 2048 + k * 1024); } while (0)
; #define PG8_LDB(dst, b, h) do { _Pragma("unroll") for (int n = 0; n < 2; ++n) _Pragma("unroll") for (int k = 0; k < 2; ++k) dst[n][k] = *(const PG8_LAS bf16x8*)(lds + PG8_SB(b, h) + boff + n * 2048 + k * 1024); } while (0)
; #define PG8_WAIT_V(n) asm volatile("s_waitcnt vmcnt(" #n ")" ::: "memory")
; #define PG8_WAIT_L(n) asm volatile("s_waitcnt lgkmcnt(" #n ")" ::: "memory")
; #define PG8_BAR __builtin_amdgcn_s_barrier()
; #define PG8_SCHED __builtin_amdgcn_sched_barrier(0)
; template <class Epi, class Sched, bool ALIGN_EPI>
; __device__ __forceinline__ void gemm_phase(PG8_LAS unsigned char* lds, const Gemm g, const Sched& S, const Epi& E, const int tid) {
;     ...
;         const bool has_next = S.next(ui + 1, nxt);
;         const char* nA = has_next ? (const char*)g.A + (size_t)nxt.pm * tstepA + PG8_ACOL(nxt) : cA; const char* nB = has_next ? (const char*)g.Bt + (size_t)nxt.pn * tstepB : cB;
;         for (int t = 0; t < nt; t += 2) {
;             const bool last = (t == nt - 2);
;             const char* a1 = cA + (size_t)(t + 1) * kstepA;
;             const char* a2 = last ? nA : cA + (size_t)(t + 2) * kstepA; const char* b2 = last ? nB : cB + (size_t)(t + 2) * kstepB;
;             const char* a3 = a2 + kstepA; const char* b3 = b2 + kstepB;
;             if (last && has_next) S.a_ready(nxt);
;             PG8_LDB(B0, 0, 0); PG8_LDB(B1, 0, 1); PG8_SCHED; PG8_LDA(At, 0, 0); PG8_STAGE(PG8_SA(1, 1), a1 + hstepA, voffA);
;             PG8_WAIT_V(8); PG8_WAIT_L(0); PG8_BAR; PG8_MMA(0, 0, At, B0); PG8_MMA(0, 1, At, B1); PG8_BAR; PG8_SCHED;
;             PG8_LDA(At, 0, 1); PG8_STAGE(PG8_SB(0, 0), b2, voffB); PG8_STAGE(PG8_SB(0, 1), b2 + hstepB, voffB); PG8_STAGE(PG8_SA(0, 0), a2, voffA);
;             PG8_WAIT_V(8); PG8_WAIT_L(0); PG8_BAR; PG8_MMA(1, 0, At, B0); PG8_MMA(1, 1, At, B1); PG8_BAR; PG8_SCHED;
.LBB0_341:
	s_ashr_i32 s47, s46, 31
	s_lshl_b64 s[48:49], s[46:47], 20
	s_add_u32 s48, s57, s48
	s_addc_u32 s49, s58, s49
	s_and_b64 s[50:51], s[6:7], exec
	s_cselect_b32 s9, s49, s11
	s_cselect_b32 s43, s48, s10
	s_ashr_i32 s45, s44, 31
	s_lshl_b64 s[50:51], s[44:45], 20
	s_add_u32 s50, s56, s50
	s_addc_u32 s51, s33, s51
	s_and_b64 s[52:53], s[6:7], exec
	s_cselect_b32 s45, s51, s13
	s_cselect_b32 s47, s50, s12
	s_add_u32 s10, s10, 0xc000
	s_addc_u32 s11, s11, 0
	s_add_u32 s79, s12, 0x10000
	s_addc_u32 s80, s13, 0
	s_mov_b32 s81, -2
	s_waitcnt lgkmcnt(0)
	s_waitcnt vmcnt(0)
	v_add_u32_e32 v166, 0x10000, v171
	s_add_u32 s12, s10, 0x4000
	s_addc_u32 s13, s11, 0
	s_cmp_eq_u32 s81, 28
	s_cselect_b32 s54, s43, s12
	s_cselect_b32 s55, s9, s13
	s_cselect_b32 s52, s47, s79
	s_cselect_b32 s53, s45, s80
	s_add_u32 s12, s54, 0x8000
	s_addc_u32 s13, s55, 0
	s_add_i32 s82, 0, 0x10000
	s_add_i32 s84, 0, 0x14000
	ds_read_b128 v[48:51], v166
	ds_read_b128 v[52:55], v166 offset:1024
	ds_read_b128 v[64:67], v166 offset:2048
	ds_read_b128 v[68:71], v166 offset:3072
	ds_read_b128 v[146:149], v166 offset:16384
	ds_read_b128 v[150:153], v166 offset:17408
	ds_read_b128 v[180:183], v166 offset:18432
	ds_read_b128 v[184:187], v166 offset:19456
	s_add_i32 m0, s62, 0xc000
	ds_read_b128 v[188:191], v210
	ds_read_b128 v[192:195], v210 offset:1024
	ds_read_b128 v[196:199], v210 offset:2048
	ds_read_b128 v[200:203], v210 offset:3072
	ds_read_b128 v[204:207], v210 offset:4096
	ds_read_b128 v[212:215], v210 offset:5120
	ds_read_b128 v[216:219], v210 offset:6144
	ds_read_b128 v[220:223], v210 offset:7168
	global_load_lds_dwordx4 v176, s[10:11]
	s_add_i32 m0, s62, 0xe000
	s_nop 0
	global_load_lds_dwordx4 v178, s[10:11]
	s_waitcnt vmcnt(8)
	s_waitcnt lgkmcnt(0)
	s_setprio 1
	s_barrier
	v_mfma_f32_16x16x32_bf16 v[142:145], v[48:51], v[188:191], 0
	v_mfma_f32_16x16x32_bf16 v[138:141], v[64:67], v[188:191], 0
	v_mfma_f32_16x16x32_bf16 v[124:127], v[48:51], v[196:199], 0
	v_mfma_f32_16x16x32_bf16 v[120:123], v[64:67], v[196:199], 0
	v_mfma_f32_16x16x32_bf16 v[108:111], v[48:51], v[204:207], 0
	v_mfma_f32_16x16x32_bf16 v[104:107], v[64:67], v[204:207], 0
	v_mfma_f32_16x16x32_bf16 v[92:95], v[48:51], v[216:219], 0
	v_mfma_f32_16x16x32_bf16 v[88:91], v[64:67], v[216:219], 0
	v_mfma_f32_16x16x32_bf16 v[142:145], v[52:55], v[192:195], v[142:145]
	v_mfma_f32_16x16x32_bf16 v[138:141], v[68:71], v[192:195], v[138:141]
	v_mfma_f32_16x16x32_bf16 v[124:127], v[52:55], v[200:203], v[124:127]
	v_mfma_f32_16x16x32_bf16 v[120:123], v[68:71], v[200:203], v[120:123]
	v_mfma_f32_16x16x32_bf16 v[108:111], v[52:55], v[212:215], v[108:111]
	v_mfma_f32_16x16x32_bf16 v[104:107], v[68:71], v[212:215], v[104:107]
	v_mfma_f32_16x16x32_bf16 v[92:95], v[52:55], v[220:223], v[92:95]
	v_mfma_f32_16x16x32_bf16 v[88:91], v[68:71], v[220:223], v[88:91]
	v_mfma_f32_16x16x32_bf16 v[134:137], v[146:149], v[188:191], 0
	v_mfma_f32_16x16x32_bf16 v[130:133], v[180:183], v[188:191], 0
	v_mfma_f32_16x16x32_bf16 v[116:119], v[146:149], v[196:199], 0
	v_mfma_f32_16x16x32_bf16 v[112:115], v[180:183], v[196:199], 0
	v_mfma_f32_16x16x32_bf16 v[100:103], v[146:149], v[204:207], 0
	v_mfma_f32_16x16x32_bf16 v[96:99], v[180:183], v[204:207], 0
	v_mfma_f32_16x16x32_bf16 v[84:87], v[146:149], v[216:219], 0
	v_mfma_f32_16x16x32_bf16 v[80:83], v[180:183], v[216:219], 0
	v_mfma_f32_16x16x32_bf16 v[134:137], v[150:153], v[192:195], v[134:137]
	v_mfma_f32_16x16x32_bf16 v[130:133], v[184:187], v[192:195], v[130:133]
	v_mfma_f32_16x16x32_bf16 v[116:119], v[150:153], v[200:203], v[116:119]
	v_mfma_f32_16x16x32_bf16 v[112:115], v[184:187], v[200:203], v[112:115]
	v_mfma_f32_16x16x32_bf16 v[100:103], v[150:153], v[212:215], v[100:103]
	v_mfma_f32_16x16x32_bf16 v[96:99], v[184:187], v[212:215], v[96:99]
	v_mfma_f32_16x16x32_bf16 v[84:87], v[150:153], v[220:223], v[84:87]
	v_mfma_f32_16x16x32_bf16 v[80:83], v[184:187], v[220:223], v[80:83]
	s_barrier
	s_setprio 0
	s_add_i32 s82, s82, s59
	s_mov_b32 m0, s82
	ds_read_b128 v[188:191], v210 offset:16384
	ds_read_b128 v[192:195], v210 offset:17408
	ds_read_b128 v[196:199], v210 offset:18432
	ds_read_b128 v[200:203], v210 offset:19456
	ds_read_b128 v[204:207], v210 offset:20480
	ds_read_b128 v[212:215], v210 offset:21504
	ds_read_b128 v[216:219], v210 offset:22528
	ds_read_b128 v[220:223], v210 offset:23552
	global_load_lds_dwordx4 v156, s[52:53]
	s_add_i32 m0, s82, 0x2000
	s_add_u32 s82, s52, 0x4000
	s_addc_u32 s83, s53, 0
	s_add_i32 s84, s84, s59
	global_load_lds_dwordx4 v160, s[52:53]
	s_mov_b32 m0, s84
	s_nop 0
	global_load_lds_dwordx4 v156, s[82:83]
	s_add_i32 m0, s84, 0x2000
	s_nop 0
	global_load_lds_dwordx4 v160, s[82:83]
	s_mov_b32 m0, s62
	s_nop 0
	global_load_lds_dwordx4 v154, s[54:55]
	s_mov_b32 m0, s63
	s_nop 0
	global_load_lds_dwordx4 v158, s[54:55]
	s_waitcnt vmcnt(8)
	s_waitcnt lgkmcnt(0)
	s_setprio 1
	s_barrier
; #define PG8_STAGE(bufoff, gbase, voff) do { _Pragma("unroll") for (int _i = 0; _i < 2; ++_i) \
;         __builtin_amdgcn_global_load_lds((const unsigned*)((const char*)(gbase) + (voff)[_i]), (PG8_LAS unsigned*)(lds + (bufoff) + ldsw + _i * 8192), 16, 0, 0); } while (0)
; #define PG8_LDA(dst, b, h) do { _Pragma("unroll") for (int m = 0; m < 4; ++m) _Pragma("unroll") for (int k = 0; k < 2; ++k) dst[m][k] = *(const PG8_LAS bf16x8*)(lds + PG8_SA(b, h) + aoff + m * 2048 + k * 1024); } while (0)
; #define PG8_LDB(dst, b, h) do { _Pragma("unroll") for (int n = 0; n < 2; ++n) _Pragma("unroll") for (int k = 0; k < 2; ++k) dst[n][k] = *(const PG8_LAS bf16x8*)(lds + PG8_SB(b, h) + boff + n * 2048 + k * 1024); } while (0)
; #define PG8_MMA(ai, bj, At, Bt) do { __builtin_amdgcn_s_setprio(1); _Pragma("unroll") for (int m = 0; m < 4; ++m) _Pragma("unroll") for (int n = 0; n < 2; ++n) _Pragma("unroll") for (int k = 0; k < 2; ++k) \
;         acc[ai][bj][m][n] = __builtin_amdgcn_mfma_f32_16x16x32_bf16(Bt[n][k], At[m][k], acc[ai][bj][m][n], 0, 0, 0); __builtin_amdgcn_s_setprio(0); } while (0)
; #define PG8_WAIT_V(n) asm volatile("s_waitcnt vmcnt(" #n ")" ::: "memory")
; #define PG8_WAIT_L(n) asm volatile("s_waitcnt lgkmcnt(" #n ")" ::: "memory")
; #define PG8_BAR __builtin_amdgcn_s_barrier()
; #define PG8_SCHED __builtin_amdgcn_sched_barrier(0)
; template <class Epi, class Sched, bool ALIGN_EPI>
; __device__ __forceinline__ void gemm_phase(PG8_LAS unsigned char* lds, const Gemm g, const Sched& S, const Epi& E, const int tid) {
;     ...
;             PG8_WAIT_V(8); PG8_WAIT_L(0); PG8_BAR; PG8_MMA(1, 0, At, B0); PG8_MMA(1, 1, At, B1); PG8_BAR; PG8_SCHED;
;             PG8_LDB(B0, 1, 0); PG8_LDB(B1, 1, 1); PG8_SCHED; PG8_LDA(At, 1, 0); PG8_STAGE(PG8_SA(0, 1), a2 + hstepA, voffA);
;             PG8_WAIT_V(8); PG8_WAIT_L(0); PG8_BAR; PG8_MMA(0, 0, At, B0); PG8_MMA(0, 1, At, B1); PG8_BAR; PG8_SCHED;
;             PG8_LDA(At, 1, 1); PG8_STAGE(PG8_SB(1, 0), b3, voffB); PG8_STAGE(PG8_SB(1, 1), b3 + hstepB, voffB); PG8_STAGE(PG8_SA(1, 0), a3, voffA);
	v_mfma_f32_16x16x32_bf16 v[76:79], v[48:51], v[188:191], 0
	v_mfma_f32_16x16x32_bf16 v[72:75], v[64:67], v[188:191], 0
	v_mfma_f32_16x16x32_bf16 v[44:47], v[48:51], v[196:199], 0
	v_mfma_f32_16x16x32_bf16 v[40:43], v[64:67], v[196:199], 0
	v_mfma_f32_16x16x32_bf16 v[28:31], v[48:51], v[204:207], 0
	v_mfma_f32_16x16x32_bf16 v[24:27], v[64:67], v[204:207], 0
	v_mfma_f32_16x16x32_bf16 v[12:15], v[48:51], v[216:219], 0
	v_mfma_f32_16x16x32_bf16 v[8:11], v[64:67], v[216:219], 0
	v_mfma_f32_16x16x32_bf16 v[76:79], v[52:55], v[192:195], v[76:79]
	v_mfma_f32_16x16x32_bf16 v[72:75], v[68:71], v[192:195], v[72:75]
	v_mfma_f32_16x16x32_bf16 v[44:47], v[52:55], v[200:203], v[44:47]
	v_mfma_f32_16x16x32_bf16 v[40:43], v[68:71], v[200:203], v[40:43]
	v_mfma_f32_16x16x32_bf16 v[28:31], v[52:55], v[212:215], v[28:31]
	v_mfma_f32_16x16x32_bf16 v[24:27], v[68:71], v[212:215], v[24:27]
	v_mfma_f32_16x16x32_bf16 v[12:15], v[52:55], v[220:223], v[12:15]
	v_mfma_f32_16x16x32_bf16 v[8:11], v[68:71], v[220:223], v[8:11]
	v_mfma_f32_16x16x32_bf16 v[36:39], v[146:149], v[196:199], 0
	v_mfma_f32_16x16x32_bf16 v[32:35], v[180:183], v[196:199], 0
	v_mfma_f32_16x16x32_bf16 v[20:23], v[146:149], v[204:207], 0
	v_mfma_f32_16x16x32_bf16 v[16:19], v[180:183], v[204:207], 0
	v_mfma_f32_16x16x32_bf16 v[4:7], v[146:149], v[216:219], 0
	v_mfma_f32_16x16x32_bf16 v[0:3], v[180:183], v[216:219], 0
	v_mfma_f32_16x16x32_bf16 v[48:51], v[146:149], v[188:191], 0
	v_mfma_f32_16x16x32_bf16 v[52:55], v[180:183], v[188:191], 0
	v_mfma_f32_16x16x32_bf16 v[36:39], v[150:153], v[200:203], v[36:39]
	v_mfma_f32_16x16x32_bf16 v[32:35], v[184:187], v[200:203], v[32:35]
	v_mfma_f32_16x16x32_bf16 v[20:23], v[150:153], v[212:215], v[20:23]
	v_mfma_f32_16x16x32_bf16 v[16:19], v[184:187], v[212:215], v[16:19]
	v_mfma_f32_16x16x32_bf16 v[4:7], v[150:153], v[220:223], v[4:7]
	v_mfma_f32_16x16x32_bf16 v[0:3], v[184:187], v[220:223], v[0:3]
	v_mfma_f32_16x16x32_bf16 v[48:51], v[150:153], v[192:195], v[48:51]
	v_mfma_f32_16x16x32_bf16 v[52:55], v[184:187], v[192:195], v[52:55]
	s_barrier
	s_setprio 0
	s_add_i32 s82, 0, 0x18000
	s_add_i32 s83, 0, 0x1c000
	ds_read_b128 v[56:59], v166 offset:32768
	ds_read_b128 v[60:63], v166 offset:33792
	ds_read_b128 v[64:67], v166 offset:34816
	ds_read_b128 v[68:71], v166 offset:35840
	ds_read_b128 v[146:149], v166 offset:49152
	ds_read_b128 v[150:153], v166 offset:50176
	ds_read_b128 v[180:183], v166 offset:51200
	ds_read_b128 v[184:187], v166 offset:52224
	s_add_u32 s54, s54, 0x4000
	s_addc_u32 s55, s55, 0
	s_mov_b32 m0, s64
	ds_read_b128 v[188:191], v210 offset:32768
	ds_read_b128 v[192:195], v210 offset:33792
	ds_read_b128 v[196:199], v210 offset:34816
	ds_read_b128 v[200:203], v210 offset:35840
	ds_read_b128 v[204:207], v210 offset:36864
	ds_read_b128 v[212:215], v210 offset:37888
	ds_read_b128 v[216:219], v210 offset:38912
	ds_read_b128 v[220:223], v210 offset:39936
	global_load_lds_dwordx4 v154, s[54:55]
	s_mov_b32 m0, s65
	s_nop 0
	global_load_lds_dwordx4 v158, s[54:55]
	s_waitcnt vmcnt(8)
	s_waitcnt lgkmcnt(0)
	s_setprio 1
	s_barrier
	v_mfma_f32_16x16x32_bf16 v[142:145], v[56:59], v[188:191], v[142:145]
	v_mfma_f32_16x16x32_bf16 v[138:141], v[64:67], v[188:191], v[138:141]
	v_mfma_f32_16x16x32_bf16 v[124:127], v[56:59], v[196:199], v[124:127]
	v_mfma_f32_16x16x32_bf16 v[120:123], v[64:67], v[196:199], v[120:123]
	v_mfma_f32_16x16x32_bf16 v[108:111], v[56:59], v[204:207], v[108:111]
	v_mfma_f32_16x16x32_bf16 v[104:107], v[64:67], v[204:207], v[104:107]
	v_mfma_f32_16x16x32_bf16 v[92:95], v[56:59], v[216:219], v[92:95]
	v_mfma_f32_16x16x32_bf16 v[88:91], v[64:67], v[216:219], v[88:91]
	v_mfma_f32_16x16x32_bf16 v[142:145], v[60:63], v[192:195], v[142:145]
	v_mfma_f32_16x16x32_bf16 v[138:141], v[68:71], v[192:195], v[138:141]
	v_mfma_f32_16x16x32_bf16 v[124:127], v[60:63], v[200:203], v[124:127]
	v_mfma_f32_16x16x32_bf16 v[120:123], v[68:71], v[200:203], v[120:123]
	v_mfma_f32_16x16x32_bf16 v[108:111], v[60:63], v[212:215], v[108:111]
	v_mfma_f32_16x16x32_bf16 v[104:107], v[68:71], v[212:215], v[104:107]
	v_mfma_f32_16x16x32_bf16 v[92:95], v[60:63], v[220:223], v[92:95]
	v_mfma_f32_16x16x32_bf16 v[88:91], v[68:71], v[220:223], v[88:91]
	v_mfma_f32_16x16x32_bf16 v[134:137], v[146:149], v[188:191], v[134:137]
	v_mfma_f32_16x16x32_bf16 v[130:133], v[180:183], v[188:191], v[130:133]
	v_mfma_f32_16x16x32_bf16 v[116:119], v[146:149], v[196:199], v[116:119]
	v_mfma_f32_16x16x32_bf16 v[112:115], v[180:183], v[196:199], v[112:115]
	v_mfma_f32_16x16x32_bf16 v[100:103], v[146:149], v[204:207], v[100:103]
	v_mfma_f32_16x16x32_bf16 v[96:99], v[180:183], v[204:207], v[96:99]
	v_mfma_f32_16x16x32_bf16 v[84:87], v[146:149], v[216:219], v[84:87]
	v_mfma_f32_16x16x32_bf16 v[80:83], v[180:183], v[216:219], v[80:83]
	v_mfma_f32_16x16x32_bf16 v[134:137], v[150:153], v[192:195], v[134:137]
	v_mfma_f32_16x16x32_bf16 v[130:133], v[184:187], v[192:195], v[130:133]
	v_mfma_f32_16x16x32_bf16 v[116:119], v[150:153], v[200:203], v[116:119]
	v_mfma_f32_16x16x32_bf16 v[112:115], v[184:187], v[200:203], v[112:115]
	v_mfma_f32_16x16x32_bf16 v[100:103], v[150:153], v[212:215], v[100:103]
	v_mfma_f32_16x16x32_bf16 v[96:99], v[184:187], v[212:215], v[96:99]
	v_mfma_f32_16x16x32_bf16 v[84:87], v[150:153], v[220:223], v[84:87]
	v_mfma_f32_16x16x32_bf16 v[80:83], v[184:187], v[220:223], v[80:83]
	s_barrier
; #define PG8_STAGE(bufoff, gbase, voff) do { _Pragma("unroll") for (int _i = 0; _i < 2; ++_i) \
;         __builtin_amdgcn_global_load_lds((const unsigned*)((const char*)(gbase) + (voff)[_i]), (PG8_LAS unsigned*)(lds + (bufoff) + ldsw + _i * 8192), 16, 0, 0); } while (0)
; #define PG8_LDA(dst, b, h) do { _Pragma("unroll") for (int m = 0; m < 4; ++m) _Pragma("unroll") for (int k = 0; k < 2; ++k) dst[m][k] = *(const PG8_LAS bf16x8*)(lds + PG8_SA(b, h) + aoff + m * 2048 + k * 1024); } while (0)
; #define PG8_MMA(ai, bj, At, Bt) do { __builtin_amdgcn_s_setprio(1); _Pragma("unroll") for (int m = 0; m < 4; ++m) _Pragma("unroll") for (int n = 0; n < 2; ++n) _Pragma("unroll") for (int k = 0; k < 2; ++k) \
;         acc[ai][bj][m][n] = __builtin_amdgcn_mfma_f32_16x16x32_bf16(Bt[n][k], At[m][k], acc[ai][bj][m][n], 0, 0, 0); __builtin_amdgcn_s_setprio(0); } while (0)
; #define PG8_WAIT_V(n) asm volatile("s_waitcnt vmcnt(" #n ")" ::: "memory")
; #define PG8_WAIT_L(n) asm volatile("s_waitcnt lgkmcnt(" #n ")" ::: "memory")
; #define PG8_BAR __builtin_amdgcn_s_barrier()
; #define PG8_SCHED __builtin_amdgcn_sched_barrier(0)
; template <class Epi, class Sched, bool ALIGN_EPI>
; __device__ __forceinline__ void gemm_phase(PG8_LAS unsigned char* lds, const Gemm g, const Sched& S, const Epi& E, const int tid) {
;     ...
;             PG8_LDA(At, 1, 1); PG8_STAGE(PG8_SB(1, 0), b3, voffB); PG8_STAGE(PG8_SB(1, 1), b3 + hstepB, voffB); PG8_STAGE(PG8_SA(1, 0), a3, voffA);
;             PG8_WAIT_V(8); PG8_WAIT_L(0); PG8_BAR; PG8_MMA(1, 0, At, B0); PG8_MMA(1, 1, At, B1); PG8_BAR; PG8_SCHED;
	s_setprio 0
	s_add_u32 s54, s52, 0x8000
	s_addc_u32 s55, s53, 0
	s_add_i32 s82, s82, s59
	s_mov_b32 m0, s82
	ds_read_b128 v[188:191], v210 offset:49152
	ds_read_b128 v[192:195], v210 offset:50176
	ds_read_b128 v[196:199], v210 offset:51200
	ds_read_b128 v[200:203], v210 offset:52224
	ds_read_b128 v[204:207], v210 offset:53248
	ds_read_b128 v[212:215], v210 offset:54272
	ds_read_b128 v[216:219], v210 offset:55296
	ds_read_b128 v[220:223], v210 offset:56320
	global_load_lds_dwordx4 v156, s[54:55]
	s_add_i32 m0, s82, 0x2000
	s_add_u32 s52, s52, 0xc000
	s_addc_u32 s53, s53, 0
	global_load_lds_dwordx4 v160, s[54:55]
	s_add_i32 s54, s83, s59
	s_mov_b32 m0, s54
	s_nop 0
	global_load_lds_dwordx4 v156, s[52:53]
	s_add_i32 m0, s54, 0x2000
	s_nop 0
	global_load_lds_dwordx4 v160, s[52:53]
	s_mov_b32 m0, s66
	s_nop 0
	global_load_lds_dwordx4 v154, s[12:13]
	s_mov_b32 m0, s67
	s_nop 0
	global_load_lds_dwordx4 v158, s[12:13]
	s_waitcnt vmcnt(8)
	s_waitcnt lgkmcnt(0)
	s_setprio 1
	s_barrier
	v_mfma_f32_16x16x32_bf16 v[76:79], v[56:59], v[188:191], v[76:79]
	v_mfma_f32_16x16x32_bf16 v[72:75], v[64:67], v[188:191], v[72:75]
	v_mfma_f32_16x16x32_bf16 v[44:47], v[56:59], v[196:199], v[44:47]
	v_mfma_f32_16x16x32_bf16 v[40:43], v[64:67], v[196:199], v[40:43]
	v_mfma_f32_16x16x32_bf16 v[28:31], v[56:59], v[204:207], v[28:31]
	v_mfma_f32_16x16x32_bf16 v[24:27], v[64:67], v[204:207], v[24:27]
	v_mfma_f32_16x16x32_bf16 v[12:15], v[56:59], v[216:219], v[12:15]
	v_mfma_f32_16x16x32_bf16 v[8:11], v[64:67], v[216:219], v[8:11]
	v_mfma_f32_16x16x32_bf16 v[76:79], v[60:63], v[192:195], v[76:79]
	v_mfma_f32_16x16x32_bf16 v[72:75], v[68:71], v[192:195], v[72:75]
	v_mfma_f32_16x16x32_bf16 v[44:47], v[60:63], v[200:203], v[44:47]
	v_mfma_f32_16x16x32_bf16 v[40:43], v[68:71], v[200:203], v[40:43]
	v_mfma_f32_16x16x32_bf16 v[28:31], v[60:63], v[212:215], v[28:31]
	v_mfma_f32_16x16x32_bf16 v[24:27], v[68:71], v[212:215], v[24:27]
	v_mfma_f32_16x16x32_bf16 v[12:15], v[60:63], v[220:223], v[12:15]
	v_mfma_f32_16x16x32_bf16 v[8:11], v[68:71], v[220:223], v[8:11]
	v_mfma_f32_16x16x32_bf16 v[48:51], v[146:149], v[188:191], v[48:51]
	v_mfma_f32_16x16x32_bf16 v[60:63], v[150:153], v[192:195], v[48:51]
	v_mfma_f32_16x16x32_bf16 v[48:51], v[180:183], v[188:191], v[52:55]
	v_mfma_f32_16x16x32_bf16 v[36:39], v[146:149], v[196:199], v[36:39]
	v_mfma_f32_16x16x32_bf16 v[32:35], v[180:183], v[196:199], v[32:35]
	v_mfma_f32_16x16x32_bf16 v[20:23], v[146:149], v[204:207], v[20:23]
	v_mfma_f32_16x16x32_bf16 v[16:19], v[180:183], v[204:207], v[16:19]
	v_mfma_f32_16x16x32_bf16 v[4:7], v[146:149], v[216:219], v[4:7]
	v_mfma_f32_16x16x32_bf16 v[0:3], v[180:183], v[216:219], v[0:3]
	v_mfma_f32_16x16x32_bf16 v[56:59], v[184:187], v[192:195], v[48:51]
	v_mfma_f32_16x16x32_bf16 v[36:39], v[150:153], v[200:203], v[36:39]
	v_mfma_f32_16x16x32_bf16 v[32:35], v[184:187], v[200:203], v[32:35]
	v_mfma_f32_16x16x32_bf16 v[20:23], v[150:153], v[212:215], v[20:23]
	v_mfma_f32_16x16x32_bf16 v[16:19], v[184:187], v[212:215], v[16:19]
	v_mfma_f32_16x16x32_bf16 v[4:7], v[150:153], v[220:223], v[4:7]
	v_mfma_f32_16x16x32_bf16 v[0:3], v[184:187], v[220:223], v[0:3]
	s_barrier
	s_setprio 0
	s_add_i32 s81, s81, 2
	s_add_u32 s10, s10, 0x10000
	s_addc_u32 s11, s11, 0
	s_add_u32 s79, s79, 0x10000
	s_addc_u32 s80, s80, 0
